# grid barrier: XCD-last workgroup issues its L2 invalidate right behind the top-level arrival atomic (off the release chain), later invalidate L1-only
# baseline (speedup 1.0000x reference)
.LBB0_224:
	s_or_b64 exec, exec, s[10:11]
	buffer_inv sc1
	v_cvt_f32_u32_e32 v3, v0
	s_waitcnt vmcnt(0)
	v_readfirstlane_b32 s8, v2
	s_add_u32 s10, s84, 0x7500
	s_addc_u32 s11, s85, 0
	v_rcp_iflag_f32_e32 v3, v3
	v_add_u32_e32 v1, s8, v1
	v_add_u32_e32 v4, 1, v1
	s_mov_b64 s[12:13], -1
	v_mul_f32_e32 v2, 0x4f7ffffe, v3
	v_cvt_u32_f32_e32 v2, v2
	v_sub_u32_e32 v3, 0, v0
	v_mul_lo_u32 v3, v3, v2
	v_mul_hi_u32 v3, v2, v3
	v_add_u32_e32 v2, v2, v3
	v_mul_hi_u32 v2, v1, v2
	v_mul_lo_u32 v3, v2, v0
	v_sub_u32_e32 v1, v1, v3
	v_add_u32_e32 v5, 1, v2
	v_cmp_ge_u32_e32 vcc, v1, v0
	v_sub_u32_e32 v3, v1, v0
	s_nop 0
	v_cndmask_b32_e32 v2, v2, v5, vcc
	v_cndmask_b32_e32 v1, v1, v3, vcc
	v_add_u32_e32 v3, 1, v2
	v_cmp_ge_u32_e32 vcc, v1, v0
	s_nop 1
	v_cndmask_b32_e32 v2, v2, v3, vcc
	v_mul_lo_u32 v1, v0, v2
	v_add_u32_e32 v0, v1, v0
	v_cmp_ne_u32_e32 vcc, v4, v0
	v_mov_b64_e32 v[0:1], s[10:11]
	s_and_saveexec_b64 s[8:9], vcc
	s_cbranch_execz .LBB0_236
	v_mov_b32_e32 v0, 0
	global_load_dword v1, v0, s[10:11] sc1
	s_mov_b64 s[16:17], 0
	s_waitcnt vmcnt(0)
	v_cmp_eq_u32_e32 vcc, v1, v2
	s_and_saveexec_b64 s[14:15], vcc
	s_cbranch_execz .LBB0_235
	s_add_u32 s12, s84, 0x4200
	s_addc_u32 s13, s85, 0
	s_mov_b32 s26, 1
	s_branch .LBB0_228

.LBB0_238:
	s_or_b64 exec, exec, s[8:9]
	s_mov_b64 s[8:9], exec
	v_mbcnt_lo_u32_b32 v0, s8, 0
	v_mbcnt_hi_u32_b32 v0, s9, v0
	v_cmp_eq_u32_e32 vcc, 0, v0
	s_waitcnt vmcnt(0)
	buffer_inv sc0
	s_and_saveexec_b64 s[10:11], vcc
	s_cbranch_execz .LBB0_240
	s_bcnt1_i32_b64 s8, s[8:9]
	v_mov_b32_e32 v0, 0x2000
	v_mov_b32_e32 v1, s8
	global_atomic_add v0, v1, s[6:7] offset:1024

.LBB0_312:
	s_or_b64 exec, exec, s[8:9]
	buffer_inv sc1
	s_waitcnt vmcnt(0)
	v_readfirstlane_b32 s6, v3
	v_sub_u32_e32 v4, 0, v2
	s_mov_b64 s[8:9], -1
	v_add_u32_e32 v3, s6, v0
	v_cvt_f32_u32_e32 v0, v2
	v_readlane_b32 s6, v254, 9
	v_readlane_b32 s7, v254, 10
	v_rcp_iflag_f32_e32 v0, v0
	s_nop 0
	v_mul_f32_e32 v0, 0x4f7ffffe, v0
	v_cvt_u32_f32_e32 v0, v0
	v_mul_lo_u32 v4, v4, v0
	v_mul_hi_u32 v4, v0, v4
	v_add_u32_e32 v0, v0, v4
	v_mul_hi_u32 v0, v3, v0
	v_mul_lo_u32 v4, v0, v2
	v_sub_u32_e32 v4, v3, v4
	v_cmp_ge_u32_e32 vcc, v4, v2
	v_add_u32_e32 v5, 1, v0
	v_add_u32_e32 v3, 1, v3
	v_cndmask_b32_e32 v0, v0, v5, vcc
	v_sub_u32_e32 v5, v4, v2
	v_cndmask_b32_e32 v4, v4, v5, vcc
	v_cmp_ge_u32_e32 vcc, v4, v2
	v_add_u32_e32 v4, 1, v0
	s_nop 0
	v_cndmask_b32_e32 v0, v0, v4, vcc
	v_mul_lo_u32 v4, v2, v0
	v_add_u32_e32 v2, v4, v2
	v_cmp_ne_u32_e32 vcc, v3, v2
	v_mov_b64_e32 v[2:3], s[6:7]
	s_and_saveexec_b64 s[6:7], vcc
	s_cbranch_execz .LBB0_324
	v_readlane_b32 s8, v254, 9
	v_readlane_b32 s9, v254, 10
	s_mov_b64 s[10:11], 0
	s_nop 3
	global_load_dword v2, v1, s[8:9] sc1
	s_waitcnt vmcnt(0)
	v_cmp_eq_u32_e32 vcc, v2, v0
	s_and_saveexec_b64 s[8:9], vcc
	s_cbranch_execz .LBB0_323
	s_mov_b32 s24, 1
	s_branch .LBB0_316

.LBB0_326:
	s_or_b64 exec, exec, s[6:7]
	s_mov_b64 s[6:7], exec
	v_mbcnt_lo_u32_b32 v0, s6, 0
	v_mbcnt_hi_u32_b32 v0, s7, v0
	v_cmp_eq_u32_e32 vcc, 0, v0
	s_waitcnt vmcnt(0)
	buffer_inv sc0
	s_and_saveexec_b64 s[8:9], vcc
	s_cbranch_execz .LBB0_328
	s_bcnt1_i32_b64 s6, s[6:7]
	v_mov_b32_e32 v0, s6
	v_readlane_b32 s6, v254, 5
	v_readlane_b32 s7, v254, 6
	s_nop 4
	global_atomic_add v1, v0, s[6:7]

.LBB0_1590:
	s_or_b64 exec, exec, s[8:9]
	buffer_inv sc1
	s_waitcnt vmcnt(0)
	v_readfirstlane_b32 s6, v3
	v_sub_u32_e32 v4, 0, v2
	s_mov_b64 s[8:9], -1
	v_add_u32_e32 v3, s6, v0
	v_cvt_f32_u32_e32 v0, v2
	v_readlane_b32 s6, v254, 9
	v_readlane_b32 s7, v254, 10
	v_rcp_iflag_f32_e32 v0, v0
	s_nop 0
	v_mul_f32_e32 v0, 0x4f7ffffe, v0
	v_cvt_u32_f32_e32 v0, v0
	v_mul_lo_u32 v4, v4, v0
	v_mul_hi_u32 v4, v0, v4
	v_add_u32_e32 v0, v0, v4
	v_mul_hi_u32 v0, v3, v0
	v_mul_lo_u32 v4, v0, v2
	v_sub_u32_e32 v4, v3, v4
	v_cmp_ge_u32_e32 vcc, v4, v2
	v_add_u32_e32 v5, 1, v0
	v_add_u32_e32 v3, 1, v3
	v_cndmask_b32_e32 v0, v0, v5, vcc
	v_sub_u32_e32 v5, v4, v2
	v_cndmask_b32_e32 v4, v4, v5, vcc
	v_cmp_ge_u32_e32 vcc, v4, v2
	v_add_u32_e32 v4, 1, v0
	s_nop 0
	v_cndmask_b32_e32 v0, v0, v4, vcc
	v_mul_lo_u32 v4, v2, v0
	v_add_u32_e32 v2, v4, v2
	v_cmp_ne_u32_e32 vcc, v3, v2
	v_mov_b64_e32 v[2:3], s[6:7]
	s_and_saveexec_b64 s[6:7], vcc
	s_cbranch_execz .LBB0_1602
	v_readlane_b32 s8, v254, 9
	v_readlane_b32 s9, v254, 10
	s_mov_b64 s[10:11], 0
	s_nop 3
	global_load_dword v2, v1, s[8:9] sc1
	s_waitcnt vmcnt(0)
	v_cmp_eq_u32_e32 vcc, v2, v0
	s_and_saveexec_b64 s[8:9], vcc
	s_cbranch_execz .LBB0_1601
	s_mov_b32 s20, 1
	s_branch .LBB0_1594

.LBB0_1604:
	s_or_b64 exec, exec, s[6:7]
	s_mov_b64 s[6:7], exec
	v_mbcnt_lo_u32_b32 v0, s6, 0
	v_mbcnt_hi_u32_b32 v0, s7, v0
	v_cmp_eq_u32_e32 vcc, 0, v0
	s_waitcnt vmcnt(0)
	buffer_inv sc0
	s_and_saveexec_b64 s[8:9], vcc
	s_cbranch_execnz .LBB0_1605
	s_getpc_b64 s[98:99]
